# P12 up-GEMM unit order: one XCD serves 4 column tiles x 8 blocks per round (was 2 x 16), on top of previous best
# baseline (speedup 1.0000x reference)
; __global__ void __launch_bounds__(NTHR, 2) fwd(Args args) {
;     ...
;         { int tokv[MAXU / 2];
; #pragma unroll
;           for (int k = 0; k < MAXU / 2; ++k) { const int i = 2 * k + (tid >> 8), L = i * NG + bx, r = tid & 255; int v = 0;
;               if (L < NBt * 16) { const int blk = L >> 4, e = blkE[blk], j = blkE[160 + blk]; if (r < blkE[320 + blk]) v = WSP(int, WS_LIST)[(size_t)e * T + j * 256 + r]; }
;               tokv[k] = v; }
.LBB0_1491:
	s_or_b64 exec, exec, s[4:5]
	s_add_i32 s0, 0, 0x23380
	v_mov_b32_e32 v0, s0
	s_waitcnt lgkmcnt(0)
	s_barrier
	ds_read_b32 v0, v0
	v_ashrrev_i32_e32 v1, 8, v2
	v_mul_lo_u32 v1, v1, s83
	v_add_u32_e32 v3, s92, v1
	v_mov_b32_e32 v1, 0
	s_waitcnt lgkmcnt(0)
	v_readfirstlane_b32 s0, v0
	s_lshl_b32 s68, s0, 4
	s_add_u32 s0, s78, 0x23cc8000
	s_addc_u32 s1, s79, 0
	v_mov_b32_e32 v0, 0
	v_cmp_gt_i32_e32 vcc, s68, v3
	s_and_saveexec_b64 s[4:5], vcc
	s_cbranch_execz .LBB0_1495
	v_or_b32_e32 v20, 0xff, v3
	v_cmp_gt_i32_e32 vcc, s68, v20
	v_lshrrev_b32_e32 v20, 8, v3
	v_bfe_u32 v21, v3, 2, 1
	v_lshlrev_b32_e32 v20, 4, v20
	v_lshl_add_u32 v20, v21, 3, v20
	v_bfe_u32 v21, v3, 5, 3
	v_add_u32_e32 v20, v20, v21
	v_ashrrev_i32_e32 v21, 4, v3
	v_cndmask_b32_e32 v1, v21, v20, vcc
	s_add_i32 s2, 0, 0x22c00
	v_lshl_add_u32 v4, v1, 2, s2
	ds_read_b32 v1, v4 offset:1280
	s_waitcnt lgkmcnt(0)
	v_cmp_lt_i32_sdwa s[8:9], v2, v1 src0_sel:BYTE_0 src1_sel:DWORD
	v_mov_b32_e32 v1, 0
	s_and_saveexec_b64 s[6:7], s[8:9]
	s_cbranch_execz .LBB0_1494
	ds_read2_b32 v[4:5], v4 offset1:160
	v_mov_b32_e32 v1, 2
	s_waitcnt lgkmcnt(0)
	v_ashrrev_i32_e32 v7, 31, v4
	v_mov_b32_e32 v6, v4
	v_lshlrev_b32_e32 v4, 8, v5
	v_lshlrev_b64 v[6:7], 15, v[6:7]
	v_ashrrev_i32_e32 v5, 31, v4
	v_lshl_add_u64 v[6:7], s[0:1], 0, v[6:7]
	v_lshl_add_u64 v[4:5], v[4:5], 2, v[6:7]
	v_lshlrev_b32_sdwa v6, v1, v2 dst_sel:DWORD dst_unused:UNUSED_PAD src0_sel:DWORD src1_sel:BYTE_0
	v_mov_b32_e32 v7, 0
	v_lshl_add_u64 v[4:5], v[4:5], 0, v[6:7]
	global_load_dword v1, v[4:5], off

; __global__ void __launch_bounds__(NTHR, 2) fwd(Args args) {
;     ...
;         { int tokv[MAXU / 2];
; #pragma unroll
;           for (int k = 0; k < MAXU / 2; ++k) { const int i = 2 * k + (tid >> 8), L = i * NG + bx, r = tid & 255; int v = 0;
;               if (L < NBt * 16) { const int blk = L >> 4, e = blkE[blk], j = blkE[160 + blk]; if (r < blkE[320 + blk]) v = WSP(int, WS_LIST)[(size_t)e * T + j * 256 + r]; }
;               tokv[k] = v; }
.LBB0_1495:
	s_or_b64 exec, exec, s[4:5]
	s_lshl_b32 s2, s83, 1
	v_add_u32_e32 v3, s2, v3
	v_cmp_gt_i32_e32 vcc, s68, v3
	s_and_saveexec_b64 s[4:5], vcc
	s_cbranch_execz .LBB0_1499
	v_or_b32_e32 v20, 0xff, v3
	v_cmp_gt_i32_e32 vcc, s68, v20
	v_lshrrev_b32_e32 v20, 8, v3
	v_bfe_u32 v21, v3, 2, 1
	v_lshlrev_b32_e32 v20, 4, v20
	v_lshl_add_u32 v20, v21, 3, v20
	v_bfe_u32 v21, v3, 5, 3
	v_add_u32_e32 v20, v20, v21
	v_ashrrev_i32_e32 v21, 4, v3
	v_cndmask_b32_e32 v0, v21, v20, vcc
	s_add_i32 s6, 0, 0x22c00
	v_lshl_add_u32 v4, v0, 2, s6
	ds_read_b32 v0, v4 offset:1280
	s_waitcnt lgkmcnt(0)
	v_cmp_lt_i32_sdwa s[8:9], v2, v0 src0_sel:BYTE_0 src1_sel:DWORD
	v_mov_b32_e32 v0, 0
	s_and_saveexec_b64 s[6:7], s[8:9]
	s_cbranch_execz .LBB0_1498
	ds_read2_b32 v[4:5], v4 offset1:160
	v_mov_b32_e32 v0, 2
	s_waitcnt lgkmcnt(0)
	v_ashrrev_i32_e32 v7, 31, v4
	v_mov_b32_e32 v6, v4
	v_lshlrev_b32_e32 v4, 8, v5
	v_lshlrev_b64 v[6:7], 15, v[6:7]
	v_ashrrev_i32_e32 v5, 31, v4
	v_lshl_add_u64 v[6:7], s[0:1], 0, v[6:7]
	v_lshl_add_u64 v[4:5], v[4:5], 2, v[6:7]
	v_lshlrev_b32_sdwa v6, v0, v2 dst_sel:DWORD dst_unused:UNUSED_PAD src0_sel:DWORD src1_sel:BYTE_0
	v_mov_b32_e32 v7, 0
	v_lshl_add_u64 v[4:5], v[4:5], 0, v[6:7]
	global_load_dword v0, v[4:5], off

; __global__ void __launch_bounds__(NTHR, 2) fwd(Args args) {
;     ...
;         { int tokv[MAXU / 2];
; #pragma unroll
;           for (int k = 0; k < MAXU / 2; ++k) { const int i = 2 * k + (tid >> 8), L = i * NG + bx, r = tid & 255; int v = 0;
;               if (L < NBt * 16) { const int blk = L >> 4, e = blkE[blk], j = blkE[160 + blk]; if (r < blkE[320 + blk]) v = WSP(int, WS_LIST)[(size_t)e * T + j * 256 + r]; }
;               tokv[k] = v; }
.LBB0_1499:
	s_or_b64 exec, exec, s[4:5]
	v_add_u32_e32 v5, s2, v3
	v_cmp_gt_i32_e32 vcc, s68, v5
	v_mov_b32_e32 v3, 0
	v_mov_b32_e32 v4, 0
	s_and_saveexec_b64 s[4:5], vcc
	s_cbranch_execz .LBB0_1503
	v_or_b32_e32 v20, 0xff, v5
	v_cmp_gt_i32_e32 vcc, s68, v20
	v_lshrrev_b32_e32 v20, 8, v5
	v_bfe_u32 v21, v5, 2, 1
	v_lshlrev_b32_e32 v20, 4, v20
	v_lshl_add_u32 v20, v21, 3, v20
	v_bfe_u32 v21, v5, 5, 3
	v_add_u32_e32 v20, v20, v21
	v_ashrrev_i32_e32 v21, 4, v5
	v_cndmask_b32_e32 v4, v21, v20, vcc
	s_add_i32 s6, 0, 0x22c00
	v_lshl_add_u32 v6, v4, 2, s6
	ds_read_b32 v4, v6 offset:1280
	s_waitcnt lgkmcnt(0)
	v_cmp_lt_i32_sdwa s[8:9], v2, v4 src0_sel:BYTE_0 src1_sel:DWORD
	v_mov_b32_e32 v4, 0
	s_and_saveexec_b64 s[6:7], s[8:9]
	s_cbranch_execz .LBB0_1502
	ds_read2_b32 v[6:7], v6 offset1:160
	v_mov_b32_e32 v4, 2
	s_waitcnt lgkmcnt(0)
	v_ashrrev_i32_e32 v9, 31, v6
	v_mov_b32_e32 v8, v6
	v_lshlrev_b32_e32 v6, 8, v7
	v_lshlrev_b64 v[8:9], 15, v[8:9]
	v_ashrrev_i32_e32 v7, 31, v6
	v_lshl_add_u64 v[8:9], s[0:1], 0, v[8:9]
	v_lshl_add_u64 v[6:7], v[6:7], 2, v[8:9]
	v_lshlrev_b32_sdwa v8, v4, v2 dst_sel:DWORD dst_unused:UNUSED_PAD src0_sel:DWORD src1_sel:BYTE_0
	v_mov_b32_e32 v9, 0
	v_lshl_add_u64 v[6:7], v[6:7], 0, v[8:9]
	global_load_dword v4, v[6:7], off

; __global__ void __launch_bounds__(NTHR, 2) fwd(Args args) {
;     ...
;         { int tokv[MAXU / 2];
; #pragma unroll
;           for (int k = 0; k < MAXU / 2; ++k) { const int i = 2 * k + (tid >> 8), L = i * NG + bx, r = tid & 255; int v = 0;
;               if (L < NBt * 16) { const int blk = L >> 4, e = blkE[blk], j = blkE[160 + blk]; if (r < blkE[320 + blk]) v = WSP(int, WS_LIST)[(size_t)e * T + j * 256 + r]; }
;               tokv[k] = v; }
.LBB0_1503:
	s_or_b64 exec, exec, s[4:5]
	v_add_u32_e32 v5, s2, v5
	v_cmp_gt_i32_e32 vcc, s68, v5
	s_and_saveexec_b64 s[4:5], vcc
	s_cbranch_execz .LBB0_1507
	v_or_b32_e32 v20, 0xff, v5
	v_cmp_gt_i32_e32 vcc, s68, v20
	v_lshrrev_b32_e32 v20, 8, v5
	v_bfe_u32 v21, v5, 2, 1
	v_lshlrev_b32_e32 v20, 4, v20
	v_lshl_add_u32 v20, v21, 3, v20
	v_bfe_u32 v21, v5, 5, 3
	v_add_u32_e32 v20, v20, v21
	v_ashrrev_i32_e32 v21, 4, v5
	v_cndmask_b32_e32 v3, v21, v20, vcc
	s_add_i32 s6, 0, 0x22c00
	v_lshl_add_u32 v6, v3, 2, s6
	ds_read_b32 v3, v6 offset:1280
	s_waitcnt lgkmcnt(0)
	v_cmp_lt_i32_sdwa s[8:9], v2, v3 src0_sel:BYTE_0 src1_sel:DWORD
	v_mov_b32_e32 v3, 0
	s_and_saveexec_b64 s[6:7], s[8:9]
	s_cbranch_execz .LBB0_1506
	ds_read2_b32 v[6:7], v6 offset1:160
	v_mov_b32_e32 v3, 2
	s_waitcnt lgkmcnt(0)
	v_ashrrev_i32_e32 v9, 31, v6
	v_mov_b32_e32 v8, v6
	v_lshlrev_b32_e32 v6, 8, v7
	v_lshlrev_b64 v[8:9], 15, v[8:9]
	v_ashrrev_i32_e32 v7, 31, v6
	v_lshl_add_u64 v[8:9], s[0:1], 0, v[8:9]
	v_lshl_add_u64 v[6:7], v[6:7], 2, v[8:9]
	v_lshlrev_b32_sdwa v8, v3, v2 dst_sel:DWORD dst_unused:UNUSED_PAD src0_sel:DWORD src1_sel:BYTE_0
	v_mov_b32_e32 v9, 0
	v_lshl_add_u64 v[6:7], v[6:7], 0, v[8:9]
	global_load_dword v3, v[6:7], off

; __global__ void __launch_bounds__(NTHR, 2) fwd(Args args) {
;     ...
;         { int tokv[MAXU / 2];
; #pragma unroll
;           for (int k = 0; k < MAXU / 2; ++k) { const int i = 2 * k + (tid >> 8), L = i * NG + bx, r = tid & 255; int v = 0;
;               if (L < NBt * 16) { const int blk = L >> 4, e = blkE[blk], j = blkE[160 + blk]; if (r < blkE[320 + blk]) v = WSP(int, WS_LIST)[(size_t)e * T + j * 256 + r]; }
;               tokv[k] = v; }
.LBB0_1507:
	s_or_b64 exec, exec, s[4:5]
	v_add_u32_e32 v7, s2, v5
	v_cmp_gt_i32_e32 vcc, s68, v7
	v_mov_b32_e32 v5, 0
	v_mov_b32_e32 v6, 0
	s_and_saveexec_b64 s[4:5], vcc
	s_cbranch_execz .LBB0_1511
	v_or_b32_e32 v20, 0xff, v7
	v_cmp_gt_i32_e32 vcc, s68, v20
	v_lshrrev_b32_e32 v20, 8, v7
	v_bfe_u32 v21, v7, 2, 1
	v_lshlrev_b32_e32 v20, 4, v20
	v_lshl_add_u32 v20, v21, 3, v20
	v_bfe_u32 v21, v7, 5, 3
	v_add_u32_e32 v20, v20, v21
	v_ashrrev_i32_e32 v21, 4, v7
	v_cndmask_b32_e32 v6, v21, v20, vcc
	s_add_i32 s2, 0, 0x22c00
	v_lshl_add_u32 v7, v6, 2, s2
	ds_read_b32 v6, v7 offset:1280
	s_waitcnt lgkmcnt(0)
	v_cmp_lt_i32_sdwa s[8:9], v2, v6 src0_sel:BYTE_0 src1_sel:DWORD
	v_mov_b32_e32 v6, 0
	s_and_saveexec_b64 s[6:7], s[8:9]
	s_cbranch_execz .LBB0_1510
	ds_read2_b32 v[6:7], v7 offset1:160
	v_mov_b32_e32 v10, 2
	s_waitcnt lgkmcnt(0)
	v_ashrrev_i32_e32 v9, 31, v6
	v_mov_b32_e32 v8, v6
	v_lshlrev_b32_e32 v6, 8, v7
	v_lshlrev_b64 v[8:9], 15, v[8:9]
	v_ashrrev_i32_e32 v7, 31, v6
	v_lshl_add_u64 v[8:9], s[0:1], 0, v[8:9]
	v_lshl_add_u64 v[6:7], v[6:7], 2, v[8:9]
	v_lshlrev_b32_sdwa v8, v10, v2 dst_sel:DWORD dst_unused:UNUSED_PAD src0_sel:DWORD src1_sel:BYTE_0
	v_mov_b32_e32 v9, 0
	v_lshl_add_u64 v[6:7], v[6:7], 0, v[8:9]
	global_load_dword v6, v[6:7], off

;     __device__ __forceinline__ bool next(int i, Unit& u) const { const int L = i * G + c; if (L >= NB * nN) return false; u.z = L / nN; u.pn = L % nN; u.pm = i; return true; }
; __global__ void __launch_bounds__(NTHR, 2) fwd(Args args) {
;     ...
; #pragma unroll
;           for (int k = 0; k < MAXU / 2; ++k) tokTab[(2 * k + (tid >> 8)) * 256 + (tid & 255)] = tokv[k]; }
;         __syncthreads();
.LBB0_1511:
	s_or_b64 exec, exec, s[4:5]
	v_and_b32_e32 v7, 0x3fffff00, v2
	v_mov_b32_e32 v8, 2
	s_add_i32 s4, 0, 0x20400
	v_lshlrev_b32_e32 v7, 2, v7
	v_lshlrev_b32_sdwa v2, v8, v2 dst_sel:DWORD dst_unused:UNUSED_PAD src0_sel:DWORD src1_sel:BYTE_0
	v_add3_u32 v2, s4, v7, v2
	s_waitcnt vmcnt(0)
	ds_write2st64_b32 v2, v1, v0 offset1:8
	ds_write2st64_b32 v2, v4, v3 offset0:16 offset1:24
	ds_write_b32 v2, v6 offset:8192
	s_waitcnt lgkmcnt(0)
	s_barrier
	s_cmp_lt_i32 s92, s68
	v_mbcnt_lo_u32_b32 v0, -1, v5
	v_mbcnt_hi_u32_b32 v0, -1, v0
	v_add_u32_e32 v4, s94, v0
	s_cselect_b64 s[0:1], -1, 0
	s_cmp_ge_i32 s92, s68
	v_readfirstlane_b32 s2, v4
	s_cbranch_scc1 .LBB0_1514
	s_lshr_b32 s38, s92, 3
	s_and_b32 s40, s38, 3
	s_lshr_b32 s38, s38, 2
	s_and_b32 s5, s92, 3
	s_lshl_b32 s5, s5, 2
	s_or_b32 s40, s40, s5
	s_bfe_u32 s5, s92, 0x10002
	s_lshl_b32 s5, s5, 3
	s_add_i32 s38, s38, s5
	s_andn2_b64 vcc, exec, s[0:1]
	s_cbranch_vccz .LBB0_1515

; template <class Epi, class Sched, bool ALIGN_EPI = false, bool SP2 = false>
; __device__ __forceinline__ void gemm_phase(PG8_LAS unsigned char* lds, const Geo geo, const Sched& S, const Epi& E, const int wave_) {
;     ...
;         const bool has_next = S.next(ui + 1, nxt);
;     __device__ __forceinline__ bool next(int i, Unit& u) const { const int L = i * G + c; if (L >= NB * nN) return false; u.z = L / nN; u.pn = L % nN; u.pm = i; return true; }
.LBB0_1520:
	s_add_i32 s26, s26, 1
	s_mul_i32 s0, s26, s83
	s_add_i32 s0, s0, s92
	s_cmp_lt_i32 s0, s68
	s_cselect_b64 s[42:43], -1, 0
	s_cmp_ge_i32 s0, s68
	s_cbranch_scc1 .LBB0_1522
	s_or_b32 s1, s0, 0xff
	s_cmp_lt_i32 s1, s68
	s_cbranch_scc0 .Lp12b_old
	s_bfe_u32 s27, s0, 0x50003
	s_and_b32 s34, s27, 3
	s_lshr_b32 s27, s27, 2
	s_and_b32 s1, s0, 3
	s_lshl_b32 s1, s1, 2
	s_or_b32 s34, s34, s1
	s_bfe_u32 s1, s0, 0x10002
	s_lshl_b32 s1, s1, 3
	s_add_i32 s27, s27, s1
	s_lshr_b32 s1, s0, 8
	s_lshl_b32 s1, s1, 4
	s_add_i32 s27, s27, s1
	s_branch .Lp12b_done
.Lp12b_old:
	s_ashr_i32 s27, s0, 4
	s_and_b32 s34, s0, 15
.Lp12b_done:
	s_mov_b32 s33, s26
